# fix: conversion-first workgroups' MLA copy used a V-fragment ring register that aliased its second P fragment; now uses that copy's own free buffer
# speedup vs baseline: 1.0096x; 1.0016x over previous
; template <bool MLA>
; __device__ __forceinline__ void attn_unit(const P& p, LAS unsigned char* lds, const int b, const int h, const int qb) {
;     ...
;                 l_run = l_run * alpha + ps;
;                 if (__any(alpha < 1.f)) { if (hi == 0) al[r32] = alpha; asm volatile("s_waitcnt lgkmcnt(0)" ::: "memory");
; #pragma unroll
;                     for (int r = 0; r < 16; ++r) { const float a = al[(r & 3) + 8 * (r >> 2) + 4 * hi];
; #pragma unroll
;                         for (int d0 = 0; d0 < 4; ++d0) o[d0][r] *= a; } }
;                 pf0 = packf(p0, 0); pf1 = packf(p0, 1); pf2 = packf(p1, 0); pf3 = packf(p1, 1);
;             } else {
;                 if (k0 + 63 >= qw) {
; #pragma unroll
;                     for (int r = 0; r < 16; ++r) { const int c = (r & 3) + 8 * (r >> 2); if (c >= dq) p0[r] = -__builtin_inff(); if (c + 32 >= dq) p1[r] = -__builtin_inff(); } }
;                 float lsum = 0.f; bf16x8 lf[4];
; #pragma unroll
;                 for (int g = 0; g < 4; ++g) {
;                     float Lv[8];
; #pragma unroll
;                     for (int j = 0; j < 8; ++j) { const int r = 8 * (g & 1) + j;
;                         const float z = (g < 2 ? p0[r] : p1[r]);
;                         const float t = __builtin_amdgcn_logf(1.f + __builtin_amdgcn_exp2f(-fabsf(z)));
;                         const float L = -(fmaxf(z, 0.f) + t);
;                         const float ls = fminf(z, 0.f) - t;
;                         if (g < 2) p0[r] = ls; else p1[r] = ls;
;                         Lv[j] = L; lsum += L; }
;                     u32x4 w; w.x = pk2(Lv[0], Lv[1]); w.y = pk2(Lv[2], Lv[3]); w.z = pk2(Lv[4], Lv[5]); w.w = pk2(Lv[6], Lv[7]); lf[g] = __builtin_bit_cast(bf16x8, w);
;                 }
;                 p0 = AT_MFMA(tri0, lf[0], p0); p0 = AT_MFMA(tri1, lf[1], p0); p0 = AT_MFMA(ones, lf[2], p0); p0 = AT_MFMA(ones, lf[3], p0);
;                 p1 = AT_MFMA(tri0, lf[2], p1); p1 = AT_MFMA(tri1, lf[3], p1);
; #pragma unroll
;                 for (int r = 0; r < 16; ++r) { p0[r] = __builtin_amdgcn_exp2f(p0[r] + R2); p1[r] = __builtin_amdgcn_exp2f(p1[r] + R2); }
;                 lsum += __shfl_xor(lsum, 32);
;                 R2 += lsum;
;                 pf0 = packf(p0, 0); pf1 = packf(p0, 1); pf2 = packf(p1, 0); pf3 = packf(p1, 1);
;             }
;             const LAS unsigned char* vb = kb + KT;
; #pragma unroll
.LBB0_881:
	ds_read_b128 v[108:111], v243 offset:30272
	ds_read_b128 v[224:227], v243 offset:30304
	v_cvt_pk_bf16_f32 v105, v14, v16
	v_cvt_pk_bf16_f32 v104, v10, v12
	v_cvt_pk_bf16_f32 v106, v84, v87
	v_cvt_pk_bf16_f32 v107, v98, v99
	v_cvt_pk_bf16_f32 v220, v83, v86
	v_cvt_pk_bf16_f32 v221, v88, v90
	v_cvt_pk_bf16_f32 v222, v92, v94
	v_cvt_pk_bf16_f32 v223, v101, v102
	v_cvt_pk_bf16_f32 v4, v4, v5
	v_cvt_pk_bf16_f32 v5, v6, v7
	v_cvt_pk_bf16_f32 v6, v8, v9
	v_cvt_pk_bf16_f32 v7, v11, v13
	v_cvt_pk_bf16_f32 v12, v15, v17
	v_cvt_pk_bf16_f32 v13, v82, v85
	v_cvt_pk_bf16_f32 v14, v89, v91
	v_cvt_pk_bf16_f32 v15, v93, v95
	s_waitcnt lgkmcnt(7)
	v_mfma_f32_32x32x16_bf16 v[66:81], v[104:107], v[228:231], v[66:81]
	ds_read_b128 v[228:231], v243 offset:34816
	s_waitcnt lgkmcnt(7)
	v_mfma_f32_32x32x16_bf16 v[66:81], v[220:223], v[232:235], v[66:81]
	ds_read_b128 v[232:235], v243 offset:34848
	s_waitcnt lgkmcnt(7)
	v_mfma_f32_32x32x16_bf16 v[66:81], v[4:7], v[236:239], v[66:81]
	ds_read_b128 v[236:239], v243 offset:34880
	s_waitcnt lgkmcnt(7)
	v_mfma_f32_32x32x16_bf16 v[66:81], v[12:15], v[244:247], v[66:81]
	ds_read_b128 v[244:247], v243 offset:34912
	s_waitcnt lgkmcnt(7)
	v_mfma_f32_32x32x16_bf16 v[50:65], v[104:107], v[248:251], v[50:65]
	ds_read_b128 v[248:251], v243 offset:39424
	s_waitcnt lgkmcnt(7)
	v_mfma_f32_32x32x16_bf16 v[50:65], v[220:223], v[252:255], v[50:65]
	ds_read_b128 v[252:255], v243 offset:39456
	s_waitcnt lgkmcnt(7)
	v_mfma_f32_32x32x16_bf16 v[50:65], v[4:7], v[108:111], v[50:65]
	ds_read_b128 v[108:111], v243 offset:39488
	s_waitcnt lgkmcnt(7)
	v_mfma_f32_32x32x16_bf16 v[50:65], v[12:15], v[224:227], v[50:65]
	ds_read_b128 v[224:227], v243 offset:39520
	s_waitcnt lgkmcnt(7)
	v_mfma_f32_32x32x16_bf16 v[34:49], v[104:107], v[228:231], v[34:49]
	s_waitcnt lgkmcnt(6)
	v_mfma_f32_32x32x16_bf16 v[34:49], v[220:223], v[232:235], v[34:49]
	s_waitcnt lgkmcnt(5)
	v_mfma_f32_32x32x16_bf16 v[34:49], v[4:7], v[236:239], v[34:49]
	s_waitcnt lgkmcnt(4)
	v_mfma_f32_32x32x16_bf16 v[34:49], v[12:15], v[244:247], v[34:49]
	s_waitcnt lgkmcnt(3)
	v_add_f32_e32 v17, v97, v100
	v_fmac_f32_e32 v17, v218, v96
	v_mfma_f32_32x32x16_bf16 v[18:33], v[104:107], v[248:251], v[18:33]
	s_waitcnt lgkmcnt(2)
	v_mfma_f32_32x32x16_bf16 v[18:33], v[220:223], v[252:255], v[18:33]
	s_waitcnt lgkmcnt(1)
	v_mfma_f32_32x32x16_bf16 v[18:33], v[4:7], v[108:111], v[18:33]
	s_waitcnt lgkmcnt(0)
	v_mfma_f32_32x32x16_bf16 v[18:33], v[12:15], v[224:227], v[18:33]
	v_mov_b32_e32 v218, v17
	s_andn2_b64 vcc, exec, s[86:87]
	s_cbranch_vccz .LBB0_883
	s_branch .LBB0_884
